# scan weight conversion rewritten: dwordx4 loads, in-lane bf16 packing, full-line stores
# speedup vs baseline: 1.0100x; 1.0100x over previous
.LBB0_409:
	s_mul_i32 s1, s10, 0x2200000
	v_readlane_b32 s6, v255, 11
	s_mul_hi_i32 s0, s10, 0x2200000
	s_add_u32 s6, s6, s1
	v_readlane_b32 s1, v255, 12
	s_addc_u32 s7, s1, s0
	s_lshl_b32 s42, s12, 1
	s_add_u32 s0, s16, s42
	s_addc_u32 s1, s17, 0
	s_lshl_b32 s12, s44, 3
	v_readlane_b32 s13, v255, 1
	s_add_i32 s28, s12, s13
	s_add_u32 s12, s6, s42
	s_addc_u32 s13, s7, 0
	s_lshl_b32 s6, s10, 3
	s_ashr_i32 s7, s6, 31
	s_lshl_b32 s48, s9, 12
	s_lshl_b64 s[6:7], s[6:7], 2
	v_readlane_b32 s14, v255, 9
	v_readlane_b32 s15, v255, 10
	s_add_u32 s6, s14, s6
	s_addc_u32 s7, s15, s7
	s_lshl_b32 s8, s8, 2
	s_add_u32 s6, s6, s8
	v_lshlrev_b32_e32 v3, 4, v1
	s_addc_u32 s7, s7, 0
	v_and_b32_e32 v7, 0x70, v3
	v_readlane_b32 s29, v255, 24
	v_and_b32_e32 v13, 48, v3
	v_writelane_b32 v255, s6, 32
	v_and_b32_e32 v3, 3, v1
	v_and_b32_e32 v5, 15, v1
	v_writelane_b32 v255, s7, 33
	v_cmp_eq_u32_e64 s[6:7], 0, v3
	v_readlane_b32 s9, v255, 28
	s_movk_i32 s18, 0x210
	v_writelane_b32 v255, s6, 34
	v_lshlrev_b32_e32 v14, 4, v3
	s_lshl_b32 s10, s11, 5
	v_writelane_b32 v255, s7, 35
	v_mul_lo_u32 v4, v124, s18
	v_readlane_b32 s6, v255, 18
	v_readlane_b32 s8, v255, 16
	s_movk_i32 s30, 0x50
	v_or_b32_e32 v130, s6, v5
	v_mul_lo_u32 v3, v130, s18
	s_movk_i32 s6, 0x90
	v_add_u32_e32 v15, 0, v3
	v_mul_lo_u32 v3, v130, s6
	v_readlane_b32 s6, v255, 29
	v_lshrrev_b32_e32 v2, 4, v123
	v_add_u32_e32 v9, 0, v4
	v_add_u32_e32 v133, s6, v3
	v_or_b32_e32 v3, s8, v5
	v_mul_u32_u24_e32 v134, 0x210, v3
	v_lshlrev_b32_e32 v3, 2, v1
	s_lshl_b32 s6, s11, 6
	v_and_b32_e32 v3, 12, v3
	s_add_u32 s6, s12, s6
	v_or_b32_e32 v10, s8, v3
	s_addc_u32 s7, s13, 0
	s_lshl_b32 s8, s8, 1
	v_mul_lo_u32 v4, v125, s30
	s_add_u32 s6, s6, s8
	v_add_u32_e32 v11, s29, v4
	v_add_u32_e32 v129, s9, v4
	v_lshlrev_b32_e32 v4, 2, v2
	v_lshlrev_b32_e32 v2, 3, v2
	v_lshlrev_b32_e32 v137, 1, v3
	s_addc_u32 s7, s7, 0
	v_mov_b32_e32 v3, v107
	v_lshl_add_u64 v[110:111], s[6:7], 0, v[2:3]
	v_readlane_b32 s6, v255, 17
	v_readlane_b32 s14, v255, 19
	v_lshrrev_b32_e32 v128, 5, v123
	v_lshrrev_b32_e32 v250, 3, v123
	v_and_b32_e32 v251, 7, v123
	v_lshlrev_b32_e32 v252, 16, v250
	v_lshlrev_b32_e32 v253, 4, v250
	v_lshl_or_b32 v250, v251, 4, v252
	v_lshl_or_b32 v251, v251, 9, v253
	v_add_u32_e32 v17, s6, v8
	v_readlane_b32 s6, v255, 20
	v_or_b32_e32 v132, s14, v4
	v_and_b32_e32 v108, 31, v1
	v_or_b32_e32 v4, s6, v4
	v_cmp_eq_u32_e64 s[6:7], 0, v123
	v_and_b32_e32 v131, 48, v1
	v_bfe_u32 v6, v1, 2, 2
	v_writelane_b32 v255, s6, 36
	v_lshlrev_b32_e32 v136, 1, v10
	v_and_b32_e32 v10, 32, v1
	v_writelane_b32 v255, s7, 37
	s_and_b32 s6, s28, 0x7c0
	v_or_b32_e32 v1, s6, v128
	v_cmp_gt_u32_e64 s[6:7], v132, v130
	v_lshlrev_b32_e32 v12, 11, v1
	v_or_b32_e32 v1, s14, v5
	v_writelane_b32 v255, s6, 38
	v_lshl_add_u64 v[112:113], s[0:1], 0, v[106:107]
	v_mul_u32_u24_e32 v19, 0x210, v1
	v_writelane_b32 v255, s7, 39
	v_or_b32_e32 v1, 2, v132
	v_readlane_b32 s0, v255, 23
	v_or_b32_e32 v21, 17, v132
	v_cmp_gt_u32_e64 s[16:17], v1, v130
	v_lshl_add_u32 v140, v4, 1, s0
	s_lshl_b32 s0, s10, 1
	v_or_b32_e32 v1, 3, v132
	v_cmp_gt_u32_e64 s[22:23], v21, v130
	v_or_b32_e32 v21, 18, v132
	v_writelane_b32 v255, s0, 40
	v_or_b32_e32 v3, v2, v6
	v_cmp_gt_u32_e64 s[18:19], v1, v130
	v_or_b32_e32 v1, 16, v132
	v_cmp_gt_u32_e64 s[24:25], v21, v130
	v_or_b32_e32 v21, 19, v132
	v_or_b32_e32 v2, 32, v2
	v_writelane_b32 v255, s1, 41
	v_mul_u32_u24_e32 v135, 0x210, v5
	v_add_u32_e32 v16, s9, v8
	v_cmp_eq_u32_e64 s[8:9], 0, v5
	v_add_u32_e32 v18, 0, v131
	v_lshlrev_b32_e32 v20, 1, v132
	v_cmp_gt_u32_e64 s[20:21], v1, v130
	v_cmp_gt_u32_e64 s[26:27], v21, v130
	v_lshlrev_b32_e32 v21, 1, v1
	v_mul_u32_u24_e32 v22, 0x50, v3
	v_mov_b32_e32 v1, s29
	v_lshlrev_b32_e32 v23, 1, v2
	v_or_b32_e32 v2, v2, v6
	v_mul_u32_u24_e32 v24, 0x210, v3
	v_mov_b32_e32 v66, 0
	v_and_or_b32 v5, v122, 64, v5
	v_writelane_b32 v255, s51, 42
	s_mov_b32 s49, 0
	v_cmp_lt_u32_e64 s[14:15], v132, v130
	v_mad_u32_u24 v138, v3, s30, v1
	v_mad_u32_u24 v139, v2, s30, v1
	s_bfe_u32 s50, s28, 0x50006
	v_mov_b32_e32 v2, v107
	v_mov_b32_e32 v1, v107
	v_mov_b32_e32 v4, v107
	v_mov_b32_e32 v3, v107
	v_mov_b32_e32 v6, v107
	v_add_u32_e32 v141, v9, v7
	v_add_u32_e32 v142, v11, v13
	v_lshlrev_b32_e32 v114, 1, v8
	v_lshlrev_b32_e32 v116, 2, v12
	v_lshlrev_b32_e32 v106, 2, v108
	v_add_u32_e32 v143, v129, v14
	v_add_u32_e32 v144, v133, v20
	v_add_u32_e32 v145, v133, v21
	v_add_u32_e32 v146, v133, v23
	v_add_u32_e32 v147, v16, v22
	v_add_u32_e32 v148, v17, v24
	v_lshlrev_b32_e32 v118, 1, v10
	v_add_u32_e32 v149, v15, v131
	v_add_u32_e32 v150, v18, v19
	v_lshlrev_b32_e32 v151, 2, v5
	v_writelane_b32 v255, s46, 43
	s_mov_b32 s47, 0
	s_mov_b32 s6, 0
	s_mov_b32 s7, 0
	v_mov_b32_e32 v67, v66
	v_mov_b32_e32 v68, v66
	v_mov_b32_e32 v69, v66
	v_mov_b32_e32 v70, v66
	v_mov_b32_e32 v71, v66
	v_mov_b32_e32 v72, v66
	v_mov_b32_e32 v73, v66
	v_mov_b32_e32 v78, v66
	v_mov_b32_e32 v79, v66
	v_mov_b32_e32 v80, v66
	v_mov_b32_e32 v81, v66
	v_mov_b32_e32 v74, v66
	v_mov_b32_e32 v75, v66
	v_mov_b32_e32 v76, v66
	v_mov_b32_e32 v77, v66
	v_mov_b32_e32 v82, v66
	v_mov_b32_e32 v83, v66
	v_mov_b32_e32 v84, v66
	v_mov_b32_e32 v85, v66
	v_mov_b32_e32 v86, v66
	v_mov_b32_e32 v87, v66
	v_mov_b32_e32 v88, v66
	v_mov_b32_e32 v89, v66
	v_mov_b32_e32 v5, v107
	v_mov_b32_e32 v8, v107
	v_mov_b32_e32 v7, v107
	v_mov_b32_e32 v10, v107
	v_mov_b32_e32 v9, v107
	v_mov_b32_e32 v12, v107
	v_mov_b32_e32 v11, v107
	v_mov_b32_e32 v14, v107
	v_mov_b32_e32 v13, v107
	v_mov_b32_e32 v16, v107
	v_mov_b32_e32 v15, v107
	v_mov_b32_e32 v18, v107
	v_mov_b32_e32 v17, v107
	v_mov_b32_e32 v20, v107
	v_mov_b32_e32 v19, v107
	v_mov_b32_e32 v22, v107
	v_mov_b32_e32 v21, v107
	v_mov_b32_e32 v24, v107
	v_mov_b32_e32 v23, v107
	v_mov_b32_e32 v26, v107
	v_mov_b32_e32 v25, v107
	v_mov_b32_e32 v28, v107
	v_mov_b32_e32 v27, v107
	v_mov_b32_e32 v30, v107
	v_mov_b32_e32 v29, v107
	v_mov_b32_e32 v32, v107
	v_mov_b32_e32 v31, v107
	s_waitcnt vmcnt(0)
	s_branch .LBB0_411

.LBB0_411:
	ds_write_b128 v141, v[34:37]
	ds_write_b128 v141, v[42:45] offset:33792
	ds_write_b128 v141, v[38:41] offset:128
	ds_write_b128 v141, v[46:49] offset:33920
	ds_write_b128 v141, v[50:53] offset:256
	ds_write_b128 v141, v[58:61] offset:34048
	ds_write_b128 v141, v[54:57] offset:384
	ds_write_b128 v141, v[62:65] offset:34176
	s_and_saveexec_b64 s[0:1], s[4:5]
	ds_write_b128 v142, v[94:97]
	s_or_b64 exec, exec, s[0:1]
	s_add_i32 s10, s7, 1
	s_cmpk_eq_i32 s47, 0x10c0
	s_cselect_b64 s[88:89], -1, 0
	s_and_b64 vcc, exec, s[88:89]
	s_cbranch_vccnz .LBB0_421
	v_readlane_b32 s12, v255, 25
	v_readlane_b32 s13, v255, 26
	s_mov_b64 s[0:1], -1
	s_and_b64 vcc, exec, s[12:13]
	s_cbranch_vccz .LBB0_416
	s_lshl_b32 s0, s10, 6
	s_add_i32 s28, s47, 64
	s_add_i32 s11, s0, 0xffffff00
	s_add_i32 s0, s47, 0xffffff40
	s_cmp_lt_u32 s7, 3
	s_cselect_b32 s0, s28, s0
	v_or_b32_e32 v34, s0, v123
	s_movk_i32 s0, 0xfff
	s_cselect_b32 s0, 0xff, s0
	v_sub_u32_e32 v35, s0, v34
	v_cndmask_b32_e64 v34, v35, v34, s[2:3]
	s_cselect_b32 s0, s45, s48
	v_add_u32_e32 v34, s0, v34
	v_ashrrev_i32_e32 v35, 31, v34
	v_readlane_b32 s0, v255, 32
	v_lshlrev_b64 v[34:35], 6, v[34:35]
	v_readlane_b32 s1, v255, 33
	s_nop 1
	v_lshl_add_u64 v[34:35], s[0:1], 0, v[34:35]
	global_load_dword v236, v[34:35], off
	global_load_dword v237, v[34:35], off offset:16
	s_mov_b64 s[0:1], 0
.LBB0_416:
	s_andn2_b64 vcc, exec, s[0:1]
	s_cbranch_vccnz .LBB0_418
	s_add_i32 s11, s47, 0xffffff40
	s_add_i32 s28, s47, 64
.LBB0_418:
	s_cmp_lt_u32 s7, 3
	s_cselect_b32 s11, s28, s11
	s_movk_i32 s0, 0xfff
	v_add_u32_e32 v34, s11, v124
	s_cselect_b32 s28, 0xff, s0
	v_sub_u32_e32 v35, s28, v34
	v_cndmask_b32_e64 v34, v35, v34, s[2:3]
	s_cselect_b32 s29, s45, s48
	v_add_u32_e32 v34, s29, v34
	v_ashrrev_i32_e32 v35, 31, v34
	v_lshlrev_b64 v[34:35], 12, v[34:35]
	v_lshl_add_u64 v[62:63], v[112:113], 0, v[34:35]
	global_load_dwordx4 v[34:37], v[62:63], off
	global_load_dwordx4 v[38:41], v[62:63], off offset:128
	global_load_dwordx4 v[42:45], v[62:63], off offset:2048
	global_load_dwordx4 v[46:49], v[62:63], off offset:2176
	global_load_dwordx4 v[50:53], v[62:63], off offset:256
	global_load_dwordx4 v[54:57], v[62:63], off offset:384
	global_load_dwordx4 v[58:61], v[62:63], off offset:2304
	s_nop 0
	global_load_dwordx4 v[62:65], v[62:63], off offset:2432
	v_mov_b64_e32 v[90:91], v[94:95]
	v_mov_b64_e32 v[92:93], v[96:97]
	s_and_saveexec_b64 s[0:1], s[4:5]
	s_cbranch_execz .LBB0_420
	v_add_u32_e32 v90, s11, v125
	v_sub_u32_e32 v91, s28, v90
	v_readlane_b32 s12, v255, 7
	v_cndmask_b32_e64 v90, v91, v90, s[2:3]
	v_readlane_b32 s13, v255, 8
	v_add_u32_e32 v92, s29, v90
	s_movk_i32 s11, 0x2800
	v_mov_b64_e32 v[90:91], s[12:13]
	v_readlane_b32 s12, v255, 40
	v_mad_i64_i32 v[90:91], s[28:29], v92, s11, v[90:91]
	s_mov_b32 s43, s41
	v_readlane_b32 s13, v255, 41
	v_lshl_add_u64 v[90:91], v[90:91], 0, s[42:43]
	s_mov_b32 s13, s41
	v_lshl_add_u64 v[90:91], v[90:91], 0, s[12:13]
	v_mov_b32_e32 v115, v107
	v_lshl_add_u64 v[90:91], v[90:91], 0, v[114:115]
	v_add_co_u32_e32 v90, vcc, 0x1000, v90
	s_mov_b32 s28, s12
	s_nop 0
	v_addc_co_u32_e32 v91, vcc, 0, v91, vcc
	global_load_dwordx4 v[90:93], v[90:91], off
	v_writelane_b32 v255, s28, 40
	s_nop 1
	v_writelane_b32 v255, s29, 41
.LBB0_420:
	s_or_b64 exec, exec, s[0:1]
	s_branch .LBB0_422

.LBB0_422:
	s_ashr_i32 s11, s51, 16
	s_bfe_u32 s92, s51, 0x5000b
	v_readlane_b32 s76, v254, 36
	s_cmp_eq_u32 s11, 1
	v_readlane_b32 s77, v254, 37
	v_readlane_b32 s78, v254, 38
	v_readlane_b32 s79, v254, 39
	v_readlane_b32 s80, v254, 40
	v_readlane_b32 s81, v254, 41
	v_readlane_b32 s82, v254, 42
	v_readlane_b32 s83, v254, 43
	s_cselect_b32 s0, s76, s78
	s_cselect_b32 s1, s77, s79
	v_readlane_b32 s68, v254, 44
	s_cmp_lt_u32 s51, 0x10000
	v_readlane_b32 s82, v254, 58
	v_readlane_b32 s83, v254, 59
	s_cselect_b32 s1, s83, s1
	s_cselect_b32 s0, s82, s0
	s_lshl_b32 s12, s92, 24
	s_add_u32 s28, s0, s12
	s_addc_u32 s29, s1, 0
	v_readlane_b32 s69, v254, 45
	v_readlane_b32 s70, v254, 46
	v_readlane_b32 s71, v254, 47
	v_readlane_b32 s72, v254, 48
	v_readlane_b32 s73, v254, 49
	v_readlane_b32 s74, v254, 50
	v_readlane_b32 s75, v254, 51
	s_cmp_eq_u32 s92, 0
	s_cselect_b64 s[90:91], -1, 0
	v_readlane_b32 s60, v254, 20
	v_readlane_b32 s78, v254, 54
	v_readlane_b32 s79, v254, 55
	s_and_b64 s[0:1], s[90:91], exec
	v_readlane_b32 s74, v254, 34
	v_readlane_b32 s75, v254, 35
	s_cselect_b32 s30, s74, s78
	s_cselect_b32 s31, s75, s79
	s_cmp_eq_u32 s11, 3
	s_cselect_b64 s[52:53], -1, 0
	s_and_b64 s[0:1], s[52:53], exec
	s_cselect_b32 s1, s31, s29
	s_cselect_b32 s0, s30, s28
	s_and_b32 s43, s46, 0x7e0
	s_and_b32 s98, s51, 0x7c0
	s_lshl_b32 s98, s98, 13
	s_lshl_b32 s40, s43, 2
	s_add_u32 s98, s98, s40
	s_add_u32 s100, s0, s98
	s_addc_u32 s101, s1, 0
	global_load_dwordx4 v[152:155], v250, s[100:101]
	v_add_u32_e32 v253, 0x2000, v250
	global_load_dwordx4 v[156:159], v253, s[100:101]
	v_add_u32_e32 v252, 0x4000, v250
	global_load_dwordx4 v[160:163], v252, s[100:101]
	v_add_u32_e32 v253, 0x6000, v250
	global_load_dwordx4 v[164:167], v253, s[100:101]
	v_add_u32_e32 v252, 0x8000, v250
	global_load_dwordx4 v[168:171], v252, s[100:101]
	v_add_u32_e32 v253, 0xa000, v250
	global_load_dwordx4 v[172:175], v253, s[100:101]
	v_add_u32_e32 v252, 0xc000, v250
	global_load_dwordx4 v[176:179], v252, s[100:101]
	v_add_u32_e32 v253, 0xe000, v250
	global_load_dwordx4 v[246:249], v253, s[100:101]
	s_cmp_lt_u32 s7, 30
	s_cselect_b64 s[94:95], -1, 0
	s_and_b64 s[0:1], s[94:95], exec
	s_cselect_b32 s0, s49, 0
	s_add_i32 s0, s0, s44
	s_lshl_b32 s0, s0, 3
	v_readlane_b32 s1, v255, 15
	s_add_i32 s28, s1, s0
	s_bfe_u32 s93, s28, 0x5000b
	s_ashr_i32 s57, s28, 16
	s_lshl_b32 s13, s93, 22
	s_cmp_eq_u32 s57, 3
	s_cselect_b64 s[96:97], -1, 0
	s_cmp_eq_u32 s93, 0
	s_cselect_b64 s[0:1], -1, 0
	s_lshl_b32 s34, s28, 5
	s_and_b32 s37, s34, 0x7e0
	s_and_b32 s36, s28, 0x7c0
	s_mov_b32 s38, s86
	s_cmp_gt_u32 s7, 29
	v_readlane_b32 s76, v254, 52
	v_readlane_b32 s77, v254, 53
	v_readlane_b32 s80, v254, 56
	v_readlane_b32 s81, v254, 57
	v_readlane_b32 s61, v254, 21
	v_readlane_b32 s62, v254, 22
	v_readlane_b32 s63, v254, 23
	v_readlane_b32 s64, v254, 24
	v_readlane_b32 s65, v254, 25
	v_readlane_b32 s66, v254, 26
	v_readlane_b32 s67, v254, 27
	v_readlane_b32 s68, v254, 28
	v_readlane_b32 s69, v254, 29
	v_readlane_b32 s70, v254, 30
	v_readlane_b32 s71, v254, 31
	v_readlane_b32 s72, v254, 32
	v_readlane_b32 s73, v254, 33
	s_cbranch_scc1 .LBB0_424
	v_readlane_b32 s80, v254, 36
	s_cmp_eq_u32 s57, 1
	v_readlane_b32 s81, v254, 37
	v_readlane_b32 s82, v254, 38
	v_readlane_b32 s83, v254, 39
	s_cselect_b32 s29, s80, s82
	s_cselect_b32 s30, s81, s83
	v_readlane_b32 s68, v254, 44
	s_cmp_lt_u32 s28, 0x10000
	v_readlane_b32 s82, v254, 58
	v_readlane_b32 s83, v254, 59
	s_cselect_b32 s28, s83, s30
	s_cselect_b32 s29, s82, s29
	s_lshl_b32 s30, s13, 2
	v_readlane_b32 s69, v254, 45
	v_readlane_b32 s70, v254, 46
	v_readlane_b32 s71, v254, 47
	v_readlane_b32 s72, v254, 48
	v_readlane_b32 s73, v254, 49
	v_readlane_b32 s74, v254, 50
	v_readlane_b32 s75, v254, 51
	s_add_u32 s30, s29, s30
	s_addc_u32 s31, s28, 0
	v_readlane_b32 s60, v254, 20
	v_readlane_b32 s78, v254, 54
	v_readlane_b32 s79, v254, 55
	s_and_b64 s[28:29], s[0:1], exec
	v_readlane_b32 s74, v254, 34
	v_readlane_b32 s75, v254, 35
	s_cselect_b32 s60, s74, s78
	s_cselect_b32 vcc_lo, s75, s79
	s_and_b64 s[28:29], s[96:97], exec
	s_cselect_b32 s29, vcc_lo, s31
	s_cselect_b32 s28, s60, s30
	s_lshl_b32 s98, s36, 13
	s_lshl_b32 s40, s37, 2
	s_add_u32 s98, s98, s40
	s_add_u32 s100, s28, s98
	s_addc_u32 s101, s29, 0
	global_load_dwordx4 v[2:5], v250, s[100:101]
	v_add_u32_e32 v253, 0x2000, v250
	global_load_dwordx4 v[6:9], v253, s[100:101]
	v_add_u32_e32 v252, 0x4000, v250
	global_load_dwordx4 v[10:13], v252, s[100:101]
	v_add_u32_e32 v253, 0x6000, v250
	global_load_dwordx4 v[14:17], v253, s[100:101]
	v_add_u32_e32 v252, 0x8000, v250
	global_load_dwordx4 v[18:21], v252, s[100:101]
	v_add_u32_e32 v253, 0xa000, v250
	global_load_dwordx4 v[22:25], v253, s[100:101]
	v_add_u32_e32 v252, 0xc000, v250
	global_load_dwordx4 v[26:29], v252, s[100:101]
	v_add_u32_e32 v253, 0xe000, v250
	global_load_dwordx4 v[116:119], v253, s[100:101]
	v_readlane_b32 s84, v254, 40
	v_readlane_b32 s85, v254, 41
	v_readlane_b32 s86, v254, 42
	v_readlane_b32 s87, v254, 43
	v_readlane_b32 s76, v254, 52
	v_readlane_b32 s77, v254, 53
	v_readlane_b32 s80, v254, 56
	v_readlane_b32 s81, v254, 57
	v_readlane_b32 s61, v254, 21
	v_readlane_b32 s62, v254, 22
	v_readlane_b32 s63, v254, 23
	v_readlane_b32 s64, v254, 24
	v_readlane_b32 s65, v254, 25
	v_readlane_b32 s66, v254, 26
	v_readlane_b32 s67, v254, 27
	v_readlane_b32 s68, v254, 28
	v_readlane_b32 s69, v254, 29
	v_readlane_b32 s70, v254, 30
	v_readlane_b32 s71, v254, 31
	v_readlane_b32 s72, v254, 32
	v_readlane_b32 s73, v254, 33

.LBB0_451:
	s_or_b64 exec, exec, s[28:29]
	v_readlane_b32 s28, v255, 13
	v_readlane_b32 s29, v255, 14
	s_or_b64 s[28:29], s[28:29], s[88:89]
	s_and_b64 vcc, exec, s[28:29]
	s_cbranch_vccnz .LBB0_455
	s_waitcnt vmcnt(16)
	s_mov_b32 s7, 0xbfb8aa3b
	v_mul_f32_e64 v94, |v237|, s7
	v_exp_f32_e32 v94, v94
	s_mov_b32 s28, 0x800000
	v_mov_b32_e32 v97, 0xff800000
	s_bitcmp1_b32 s10, 0
	v_add_f32_e32 v94, 1.0, v94
	v_cmp_gt_f32_e32 vcc, s28, v94
	s_mov_b32 s28, 0x3f317217
	s_cselect_b32 s7, 0x520, 0
	v_cndmask_b32_e64 v95, 0, 32, vcc
	v_ldexp_f32 v94, v94, v95
	v_log_f32_e32 v94, v94
	v_max_f32_e32 v95, v237, v237
	v_min_f32_e32 v95, 0, v95
	s_add_i32 s7, s7, 0
	v_mul_f32_e32 v96, 0x3f317217, v94
	v_fma_f32 v96, v94, s28, -v96
	v_fmac_f32_e32 v96, 0x3377d1cf, v94
	s_mov_b32 s28, 0x7f800000
	v_fmac_f32_e32 v96, 0x3f317217, v94
	v_cmp_lt_f32_e64 s[28:29], |v94|, s28
	s_add_i32 s7, s7, 0x1e040
	v_readlane_b32 s60, v255, 36
	v_cndmask_b32_e64 v94, v94, v96, s[28:29]
	v_cndmask_b32_e32 v96, 0, v120, vcc
	v_sub_f32_e32 v94, v94, v96
	v_sub_f32_e32 v94, v95, v94
	v_mov_b32_e32 v95, v107
	v_mov_b32_e32 v96, 0xff800000
	v_add_f32_dpp v94, v94, v94 row_shr:1 row_mask:0xf bank_mask:0xf bound_ctrl:1
	v_lshl_add_u32 v99, v123, 2, s7
	v_readlane_b32 s61, v255, 37
	v_add_f32_dpp v94, v94, v94 row_shr:2 row_mask:0xf bank_mask:0xf bound_ctrl:1
	s_nop 1
	v_add_f32_dpp v94, v94, v94 row_shr:4 row_mask:0xf bank_mask:0xf bound_ctrl:1
	s_nop 1
	v_add_f32_dpp v94, v94, v94 row_shr:8 row_mask:0xf bank_mask:0xf bound_ctrl:1
	s_nop 1
	v_mov_b32_dpp v95, v94 row_bcast:15 row_mask:0xa bank_mask:0xf
	v_add_f32_e32 v94, v94, v95
	v_mov_b32_e32 v95, v107
	s_nop 1
	v_mov_b32_dpp v95, v94 row_bcast:31 row_mask:0xc bank_mask:0xf
	v_add_f32_e32 v94, v94, v95
	v_sub_f32_e32 v95, v236, v94
	v_readlane_b32 s31, v94, 63
	s_nop 0
	v_mov_b32_dpp v96, v95 row_shr:1 row_mask:0xf bank_mask:0xf
	v_max_f32_e32 v96, v96, v96
	v_max_f32_e32 v96, v95, v96
	s_nop 1
	v_mov_b32_dpp v97, v96 row_shr:2 row_mask:0xf bank_mask:0xf
	v_max_f32_e32 v97, v97, v97
	v_max_f32_e32 v96, v96, v97
	v_mov_b32_e32 v97, 0xff800000
	s_nop 1
	v_mov_b32_dpp v97, v96 row_shr:4 row_mask:0xf bank_mask:0xf
	v_max_f32_e32 v97, v97, v97
	v_max_f32_e32 v96, v96, v97
	v_mov_b32_e32 v97, 0xff800000
	s_nop 1
	v_mov_b32_dpp v97, v96 row_shr:8 row_mask:0xf bank_mask:0xf
	v_max_f32_e32 v97, v97, v97
	v_max_f32_e32 v96, v96, v97
	v_mov_b32_e32 v97, 0xff800000
	s_nop 1
	v_mov_b32_dpp v97, v96 row_bcast:15 row_mask:0xa bank_mask:0xf
	v_max_f32_e32 v97, v97, v97
	v_max_f32_e32 v96, v96, v97
	v_mov_b32_e32 v97, 0xff800000
	s_nop 1
	v_mov_b32_dpp v97, v96 row_bcast:31 row_mask:0xc bank_mask:0xf
	v_max3_f32 v96, v127, v96, v97
	v_sub_f32_e32 v97, v127, v96
	v_readlane_b32 s30, v96, 63
	v_sub_f32_e64 v94, -v94, v96
	v_mul_f32_e32 v97, 0x3fb8aa3b, v97
	v_mul_f32_e32 v94, 0x3fb8aa3b, v94
	v_subrev_f32_e32 v98, s30, v95
	v_exp_f32_e32 v97, v97
	v_exp_f32_e32 v94, v94
	v_mul_f32_e32 v98, 0x3fb8aa3b, v98
	v_exp_f32_e32 v98, v98
	ds_write2st64_b32 v99, v95, v96 offset1:1
	ds_write2st64_b32 v99, v97, v94 offset0:2 offset1:3
	ds_write_b32 v99, v98 offset:1024
	s_and_saveexec_b64 s[28:29], s[60:61]
	s_cbranch_execz .LBB0_454
	v_subrev_f32_e32 v94, s30, v127
	v_mul_f32_e32 v94, 0x3fb8aa3b, v94
	v_exp_f32_e32 v94, v94
	v_mov_b32_e32 v95, s7
	ds_write_b32 v95, v94 offset:1280

.LBB0_455:
	s_lshl_b32 s7, s92, 22
	s_lshl_b32 s7, s7, 1
	s_add_u32 s7, s35, s7
	s_addc_u32 s28, s33, 0
	s_add_u32 s29, s56, s12
	s_addc_u32 s30, s39, 0
	s_cmp_eq_u32 s11, 2
	s_cselect_b32 s7, s7, s29
	s_cselect_b32 s30, s28, s30
	s_and_b64 s[28:29], s[90:91], exec
	s_mov_b32 s12, 0x2400000
	v_readlane_b32 s80, v254, 36
	s_cselect_b32 s28, s12, 0x4300000
	v_readlane_b32 s86, v254, 42
	v_readlane_b32 s87, v254, 43
	s_add_u32 s31, s86, s28
	s_addc_u32 s60, s87, 0
	s_and_b64 s[28:29], s[52:53], exec
	s_cselect_b32 s29, s60, s30
	s_cselect_b32 s28, s31, s7
	s_lshl_b32 s7, s43, 1
	s_and_b32 s30, s46, 0x60
	s_lshl_b32 s31, s11, 7
	s_and_b32 s7, s7, 0xf00
	s_or_b32 s30, s31, s30
	s_add_i32 s30, s30, s7
	s_cmp_gt_i32 s11, 1
	s_cselect_b32 s7, s43, s30
	s_ashr_i32 s11, s7, 3
	s_andn2_b32 s11, s11, 31
	s_or_b32 s30, s11, s50
	s_ashr_i32 s31, s30, 31
	s_lshl_b64 s[30:31], s[30:31], 8
	s_and_b32 s7, s7, 0xe0
	s_or_b32 s7, s30, s7
	s_mov_b32 s100, s7
	s_mov_b32 s101, s31
	s_lshl_b64 s[100:101], s[100:101], 7
	s_add_u32 s100, s100, s28
	s_addc_u32 s101, s101, s29
	s_waitcnt vmcnt(1)
	v_cvt_pk_bf16_f32 v152, v152, v156
	v_cvt_pk_bf16_f32 v156, v153, v157
	v_cvt_pk_bf16_f32 v238, v154, v158
	v_cvt_pk_bf16_f32 v242, v155, v159
	v_cvt_pk_bf16_f32 v153, v160, v164
	v_cvt_pk_bf16_f32 v157, v161, v165
	v_cvt_pk_bf16_f32 v239, v162, v166
	v_cvt_pk_bf16_f32 v243, v163, v167
	v_cvt_pk_bf16_f32 v154, v168, v172
	v_cvt_pk_bf16_f32 v158, v169, v173
	v_cvt_pk_bf16_f32 v240, v170, v174
	v_cvt_pk_bf16_f32 v244, v171, v175
	v_cvt_pk_bf16_f32 v155, v176, v246
	v_cvt_pk_bf16_f32 v159, v177, v247
	v_cvt_pk_bf16_f32 v241, v178, v248
	v_cvt_pk_bf16_f32 v245, v179, v249
	global_store_dwordx4 v251, v[152:155], s[100:101]
	global_store_dwordx4 v251, v[156:159], s[100:101] offset:128
	global_store_dwordx4 v251, v[238:241], s[100:101] offset:256
	global_store_dwordx4 v251, v[242:245], s[100:101] offset:384
	s_andn2_b64 vcc, exec, s[94:95]
	s_mov_b32 s86, s38
	v_readlane_b32 s81, v254, 37
	v_readlane_b32 s82, v254, 38
	v_readlane_b32 s83, v254, 39
	v_readlane_b32 s84, v254, 40
	v_readlane_b32 s85, v254, 41
	s_cbranch_vccnz .LBB0_410
	s_lshl_b32 s7, s13, 1
	s_add_u32 s7, s35, s7
	s_addc_u32 s11, s33, 0
	s_lshl_b32 s28, s93, 24
	s_add_u32 s28, s56, s28
	s_addc_u32 s29, s39, 0
	s_cmp_eq_u32 s57, 2
	s_cselect_b32 s7, s7, s28
	s_cselect_b32 s11, s11, s29
	s_and_b64 s[0:1], s[0:1], exec
	s_mov_b32 s0, 0x2400000
	v_readlane_b32 s72, v254, 36
	s_cselect_b32 s0, s0, 0x4300000
	v_readlane_b32 s78, v254, 42
	v_readlane_b32 s79, v254, 43
	s_add_u32 s28, s78, s0
	s_addc_u32 s29, s79, 0
	s_and_b64 s[0:1], s[96:97], exec
	s_cselect_b32 s1, s29, s11
	s_cselect_b32 s0, s28, s7
	s_lshl_b32 s7, s37, 1
	s_and_b32 s11, s34, 0x60
	s_lshl_b32 s28, s57, 7
	s_and_b32 s7, s7, 0xf00
	s_or_b32 s11, s28, s11
	s_add_i32 s11, s11, s7
	s_cmp_gt_i32 s57, 1
	s_cselect_b32 s7, s37, s11
	s_ashr_i32 s11, s7, 3
	s_andn2_b32 s11, s11, 31
	s_lshr_b32 s28, s36, 6
	s_or_b32 s28, s11, s28
	s_ashr_i32 s29, s28, 31
	s_lshl_b64 s[28:29], s[28:29], 8
	s_and_b32 s7, s7, 0xe0
	s_or_b32 s7, s28, s7
	v_readlane_b32 s73, v254, 37
	v_readlane_b32 s74, v254, 38
	v_readlane_b32 s75, v254, 39
	v_readlane_b32 s76, v254, 40
	v_readlane_b32 s77, v254, 41
	s_mov_b32 s100, s7
	s_mov_b32 s101, s29
	s_lshl_b64 s[100:101], s[100:101], 7
	s_add_u32 s100, s100, s0
	s_addc_u32 s101, s101, s1
	v_cvt_pk_bf16_f32 v2, v2, v6
	v_cvt_pk_bf16_f32 v6, v3, v7
	v_cvt_pk_bf16_f32 v238, v4, v8
	v_cvt_pk_bf16_f32 v242, v5, v9
	v_cvt_pk_bf16_f32 v3, v10, v14
	v_cvt_pk_bf16_f32 v7, v11, v15
	v_cvt_pk_bf16_f32 v239, v12, v16
	v_cvt_pk_bf16_f32 v243, v13, v17
	v_cvt_pk_bf16_f32 v4, v18, v22
	v_cvt_pk_bf16_f32 v8, v19, v23
	v_cvt_pk_bf16_f32 v240, v20, v24
	v_cvt_pk_bf16_f32 v244, v21, v25
	v_cvt_pk_bf16_f32 v5, v26, v116
	v_cvt_pk_bf16_f32 v9, v27, v117
	v_cvt_pk_bf16_f32 v241, v28, v118
	v_cvt_pk_bf16_f32 v245, v29, v119
	global_store_dwordx4 v251, v[2:5], s[100:101]
	global_store_dwordx4 v251, v[6:9], s[100:101] offset:128
	global_store_dwordx4 v251, v[238:241], s[100:101] offset:256
	global_store_dwordx4 v251, v[242:245], s[100:101] offset:384
	s_branch .LBB0_410

	.amdhsa_kernel _Z10fwd_kernel4Args
		.amdhsa_group_segment_fixed_size 0
		.amdhsa_private_segment_fixed_size 0
		.amdhsa_kernarg_size 488
		.amdhsa_user_sgpr_count 2
		.amdhsa_user_sgpr_dispatch_ptr 0
		.amdhsa_user_sgpr_queue_ptr 0
		.amdhsa_user_sgpr_kernarg_segment_ptr 1
		.amdhsa_user_sgpr_dispatch_id 0
		.amdhsa_user_sgpr_kernarg_preload_length 0
		.amdhsa_user_sgpr_kernarg_preload_offset 0
		.amdhsa_user_sgpr_private_segment_size 0
		.amdhsa_uses_dynamic_stack 0
		.amdhsa_enable_private_segment 0
		.amdhsa_system_sgpr_workgroup_id_x 1
		.amdhsa_system_sgpr_workgroup_id_y 0
		.amdhsa_system_sgpr_workgroup_id_z 0
		.amdhsa_system_sgpr_workgroup_info 0
		.amdhsa_system_vgpr_workitem_id 0
		.amdhsa_next_free_vgpr 256
		.amdhsa_next_free_sgpr 102
		.amdhsa_accum_offset 256
		.amdhsa_reserve_vcc 1
		.amdhsa_float_round_mode_32 0
		.amdhsa_float_round_mode_16_64 0
		.amdhsa_float_denorm_mode_32 3
		.amdhsa_float_denorm_mode_16_64 3
		.amdhsa_dx10_clamp 1
		.amdhsa_ieee_mode 1
		.amdhsa_fp16_overflow 0
		.amdhsa_tg_split 0
		.amdhsa_exception_fp_ieee_invalid_op 0
		.amdhsa_exception_fp_denorm_src 0
		.amdhsa_exception_fp_ieee_div_zero 0
		.amdhsa_exception_fp_ieee_overflow 0
		.amdhsa_exception_fp_ieee_underflow 0
		.amdhsa_exception_fp_ieee_inexact 0
		.amdhsa_exception_int_div_zero 0
	.end_amdhsa_kernel

amdhsa.kernels:
  - .agpr_count:     0
    .args:
      - .offset:         0
        .size:           232
        .value_kind:     by_value
      - .offset:         232
        .size:           4
        .value_kind:     hidden_block_count_x
      - .offset:         236
        .size:           4
        .value_kind:     hidden_block_count_y
      - .offset:         240
        .size:           4
        .value_kind:     hidden_block_count_z
      - .offset:         244
        .size:           2
        .value_kind:     hidden_group_size_x
      - .offset:         246
        .size:           2
        .value_kind:     hidden_group_size_y
      - .offset:         248
        .size:           2
        .value_kind:     hidden_group_size_z
      - .offset:         250
        .size:           2
        .value_kind:     hidden_remainder_x
      - .offset:         252
        .size:           2
        .value_kind:     hidden_remainder_y
      - .offset:         254
        .size:           2
        .value_kind:     hidden_remainder_z
      - .offset:         272
        .size:           8
        .value_kind:     hidden_global_offset_x
      - .offset:         280
        .size:           8
        .value_kind:     hidden_global_offset_y
      - .offset:         288
        .size:           8
        .value_kind:     hidden_global_offset_z
      - .offset:         296
        .size:           2
        .value_kind:     hidden_grid_dims
      - .offset:         352
        .size:           4
        .value_kind:     hidden_dynamic_lds_size
    .group_segment_fixed_size: 0
    .kernarg_segment_align: 8
    .kernarg_segment_size: 488
    .language:       OpenCL C
    .language_version:
      - 2
      - 0
    .max_flat_workgroup_size: 512
    .name:           _Z10fwd_kernel4Args
    .private_segment_fixed_size: 0
    .sgpr_count:     108
    .sgpr_spill_count: 110
    .symbol:         _Z10fwd_kernel4Args.kd
    .uniform_work_group_size: 1
    .uses_dynamic_stack: false
    .vgpr_count:     256
    .vgpr_spill_count: 0
    .wavefront_size: 64
